# MLA steady loops: waves 4-7 loop rotated too (back-edge before the mid-tile barrier)
# baseline (speedup 1.0000x reference)
; #define SFENCE() __builtin_amdgcn_sched_barrier(0)
; template <bool FOX>
; __device__ __forceinline__ void attn_unit(const Args& A, int b, int h, int qb, LAS char* shm, LAS float* dg) {
;     ...
;           const lds_cptr vp = vp0 + ((t - 1) % NS) * VSLOT; float sa = 0.f, sb = 0.f;
; #pragma unroll
;           for (int g = 0; g < 2 * NQ; ++g) {
;               if (!FOX && g == 0) c0 = __builtin_amdgcn_mfma_f32_32x32x16_bf16(kf[0], qr[0], negm, 0, 0, 0);
;               else if (!FOX && g == 1) c1 = __builtin_amdgcn_mfma_f32_32x32x16_bf16(kf[1], qr[0], negm, 0, 0, 0);
;               else if (g & 1) c1 = __builtin_amdgcn_mfma_f32_32x32x16_bf16(kf[g], qr[g >> 1], c1, 0, 0, 0); else c0 = __builtin_amdgcn_mfma_f32_32x32x16_bf16(kf[g], qr[g >> 1], c0, 0, 0, 0);
;               if (g < 8) { const int i = (g >> 1) + 4 * (g & 1); vlo[i] = vtr(vp + (i >> 2) * 4096 + (i & 3) * 1024); vhi[i] = vtr(vp + (i >> 2) * 4096 + (i & 3) * 1024 + 512);
;                   if (g < 4) { sa += pp0[4 * g]; sb += pp0[4 * g + 1]; sa += pp0[4 * g + 2]; sb += pp0[4 * g + 3]; } else { sa += pp1[4 * g - 16]; sb += pp1[4 * g - 15]; sa += pp1[4 * g - 14]; sb += pp1[4 * g - 13]; }
;                   asm volatile("" : "+v"(sa), "+v"(sb)); }
;               { constexpr int G0 = FOX ? 0 : 4; if (g >= G0) { const int q = 2 * (g - G0);
; #pragma unroll
;                   for (int k = 0; k < 2; ++k) { const int w = q + k; const unsigned pkd = w < 8 ? cvt_pk_bf16(pp0[2 * w], pp0[2 * w + 1]) : cvt_pk_bf16(pp1[2 * w - 16], pp1[2 * w - 15]); pw[w >> 2][w & 3] = pkd; } } }
;               SFENCE();
;           }
;           lrun += sa + sb; }
;         MASKONLY(t);
;         float rm; ROWMAX(rm);
;         bool resc = false;
;         if (__any(rm > THR)) { const float dl = fmaxf(rm, 0.f); mhat += dl;
; #pragma unroll
;             for (int r = 0; r < 16; ++r) { c0[r] -= dl; c1[r] -= dl; }
;             if constexpr (!FOX) {
; #pragma unroll
;                 for (int r = 0; r < 16; ++r) negm[r] = -mhat;
;                 asm volatile("" : "+v"(negm)); }
;             const float f = __builtin_amdgcn_exp2f(-dl); lrun *= f; if (hi == 0) wsf[r32] = f; resc = true; }
;         SFENCE();
;         { const lds_cptr kp = kp0 + ((t + 1) % NS) * KSLOT;
; #pragma unroll
;           for (int g = 0; g < 8; ++g) { const int i = (g >> 1) + 4 * (g & 1);
.Lmla_ss2_loop:
	s_waitcnt vmcnt(3)
	s_waitcnt lgkmcnt(0)
	s_barrier
	v_mfma_f32_32x32x16_bf16 v[18:33], v[186:189], v[206:209], v[18:33]
	s_add_i32 s27, s26, 1
	s_and_b32 s64, s27, 3
	s_mulk_i32 s64, 0x3000
	v_exp_f32_e32 v66, v114
	v_exp_f32_e32 v67, v115
	v_exp_f32_e32 v68, v116
	v_exp_f32_e32 v69, v117
	v_add_u32_e32 v3, s64, v248
	v_mfma_f32_32x32x16_bf16 v[34:49], v[186:189], v[194:197], v[34:49]
	v_exp_f32_e32 v70, v118
	v_exp_f32_e32 v71, v119
	v_exp_f32_e32 v72, v120
	v_exp_f32_e32 v73, v121
	ds_read_b128 v[206:209], v3
	ds_read_b128 v[194:197], v3 offset:512
	v_mfma_f32_32x32x16_bf16 v[18:33], v[182:185], v[202:205], v[18:33]
	v_exp_f32_e32 v74, v122
	v_exp_f32_e32 v75, v123
	v_exp_f32_e32 v76, v124
	v_exp_f32_e32 v77, v125
	ds_read_b128 v[202:205], v3 offset:2048
	ds_read_b128 v[186:189], v3 offset:2560
	v_mfma_f32_32x32x16_bf16 v[34:49], v[182:185], v[214:217], v[34:49]
	v_exp_f32_e32 v78, v126
	v_exp_f32_e32 v79, v127
	v_exp_f32_e32 v80, v128
	v_exp_f32_e32 v81, v129
	ds_read_b128 v[198:201], v3 offset:4096
	ds_read_b128 v[182:185], v3 offset:4608
	v_mfma_f32_32x32x16_bf16 v[18:33], v[178:181], v[210:213], v[18:33]
	v_exp_f32_e32 v50, v98
	v_exp_f32_e32 v51, v99
	v_exp_f32_e32 v52, v100
	v_exp_f32_e32 v53, v101
	ds_read_b128 v[190:193], v3 offset:6144
	ds_read_b128 v[170:173], v3 offset:6656
	v_mfma_f32_32x32x16_bf16 v[34:49], v[178:181], v[12:15], v[34:49]
	v_exp_f32_e32 v54, v102
	v_exp_f32_e32 v55, v103
	v_exp_f32_e32 v56, v104
	v_exp_f32_e32 v57, v105
	ds_read_b128 v[178:181], v3 offset:8192
	ds_read_b128 v[166:169], v3 offset:8704
	v_mfma_f32_32x32x16_bf16 v[18:33], v[218:221], v[8:11], v[18:33]
	v_exp_f32_e32 v58, v106
	v_exp_f32_e32 v59, v107
	v_exp_f32_e32 v60, v108
	v_exp_f32_e32 v61, v109
	ds_read_b128 v[174:177], v3 offset:10240
	ds_read_b128 v[162:165], v3 offset:10752
	v_mfma_f32_32x32x16_bf16 v[34:49], v[218:221], v[4:7], v[34:49]
	v_exp_f32_e32 v62, v110
	v_exp_f32_e32 v63, v111
	v_exp_f32_e32 v64, v112
	v_exp_f32_e32 v65, v113
	s_mov_b32 s26, s27
	s_cmp_eq_u32 s27, s96
	s_cbranch_scc1 .Lmla_ss_done
	s_add_i32 s64, s27, 3
	s_cmp_lt_u32 s64, s94
	s_cbranch_scc0 .Lmla_ss_back
	s_mov_b32 m0, s52
	s_waitcnt lgkmcnt(0)
	s_add_i32 s27, s42, 0x8000
	v_mfma_f32_32x32x16_bf16 v[114:129], v[206:209], v[138:141], v[82:97]
	global_load_lds_dwordx4 v[234:235], off
	s_mov_b32 m0, s53
	s_and_b32 s27, s27, 0x6000
	s_add_u32 s42, s42, 0x2000
	s_addc_u32 s43, s43, 0
	v_add_u32_e32 v3, s27, v247
	ds_read_b64_tr_b16 v[206:207], v3 offset:49152
	ds_read_b64_tr_b16 v[208:209], v3 offset:49664
	v_add_f32_e32 v4, 0, v67
	v_add_f32_e32 v5, 0, v66
	v_add_f32_e32 v4, v69, v4
	v_add_f32_e32 v5, v68, v5
	v_mfma_f32_32x32x16_bf16 v[98:113], v[194:197], v[138:141], v[82:97]
	global_load_lds_dwordx4 v[250:251], off
	ds_read_b64_tr_b16 v[194:195], v3 offset:53248
	ds_read_b64_tr_b16 v[196:197], v3 offset:53760
	v_add_f32_e32 v4, v71, v4
	v_add_f32_e32 v5, v70, v5
	v_add_f32_e32 v4, v73, v4
	v_add_f32_e32 v5, v72, v5
	v_mfma_f32_32x32x16_bf16 v[114:129], v[202:205], v[142:145], v[114:129]
	ds_read_b64_tr_b16 v[202:203], v3 offset:50176
	ds_read_b64_tr_b16 v[204:205], v3 offset:50688
	v_add_f32_e32 v4, v75, v4
	v_add_f32_e32 v5, v74, v5
	v_add_f32_e32 v4, v77, v4
	v_add_f32_e32 v5, v76, v5
	v_mfma_f32_32x32x16_bf16 v[98:113], v[186:189], v[142:145], v[98:113]
	ds_read_b64_tr_b16 v[214:215], v3 offset:54272
	ds_read_b64_tr_b16 v[216:217], v3 offset:54784
	v_add_f32_e32 v4, v79, v4
	v_add_f32_e32 v5, v78, v5
	v_add_f32_e32 v4, v81, v4
	v_add_f32_e32 v5, v80, v5
	v_mfma_f32_32x32x16_bf16 v[114:129], v[198:201], v[146:149], v[114:129]
	ds_read_b64_tr_b16 v[210:211], v3 offset:51200
	ds_read_b64_tr_b16 v[212:213], v3 offset:51712
	v_add_f32_e32 v4, v51, v4
	v_add_f32_e32 v5, v50, v5
	v_add_f32_e32 v4, v53, v4
	v_add_f32_e32 v5, v52, v5
	v_mfma_f32_32x32x16_bf16 v[98:113], v[182:185], v[146:149], v[98:113]
	ds_read_b64_tr_b16 v[12:13], v3 offset:55296
	ds_read_b64_tr_b16 v[14:15], v3 offset:55808
	v_add_f32_e32 v4, v55, v4
	v_add_f32_e32 v5, v54, v5
	v_add_f32_e32 v4, v57, v4
	v_add_f32_e32 v5, v56, v5
	v_mfma_f32_32x32x16_bf16 v[114:129], v[190:193], v[150:153], v[114:129]
	ds_read_b64_tr_b16 v[8:9], v3 offset:52224
	ds_read_b64_tr_b16 v[10:11], v3 offset:52736
	v_add_f32_e32 v4, v59, v4
	v_add_f32_e32 v16, v61, v4
	v_add_f32_e32 v4, v58, v5
	v_add_f32_e32 v17, v60, v4
	v_mfma_f32_32x32x16_bf16 v[98:113], v[170:173], v[150:153], v[98:113]
	v_lshl_add_u64 v[234:235], v[234:235], 0, s[62:63]
	s_and_b32 s64, s26, 3
	ds_read_b64_tr_b16 v[4:5], v3 offset:56320
	ds_read_b64_tr_b16 v[6:7], v3 offset:56832
	v_add_f32_e32 v3, v63, v16
	v_add_f32_e32 v16, v62, v17
	v_add_f32_e32 v3, v65, v3
	v_add_f32_e32 v16, v64, v16
	v_mfma_f32_32x32x16_bf16 v[114:129], v[178:181], v[154:157], v[114:129]
	s_mulk_i32 s64, 0x3000
	v_lshl_add_u64 v[250:251], v[232:233], 0, s[42:43]
	v_cvt_pk_bf16_f32 v178, v50, v51
	v_cvt_pk_bf16_f32 v179, v52, v53
	v_cvt_pk_bf16_f32 v186, v66, v67
	v_cvt_pk_bf16_f32 v187, v68, v69
	v_mfma_f32_32x32x16_bf16 v[98:113], v[166:169], v[154:157], v[98:113]
	s_add_i32 s52, s64, s91
	s_add_i32 s64, s42, 0x6000
	v_cvt_pk_bf16_f32 v180, v54, v55
	v_cvt_pk_bf16_f32 v181, v56, v57
	v_cvt_pk_bf16_f32 v188, v70, v71
	v_cvt_pk_bf16_f32 v189, v72, v73
	v_mfma_f32_32x32x16_bf16 v[114:129], v[174:177], v[158:161], v[114:129]
	s_and_b32 s64, s64, 0x6000
	s_add_i32 s53, s64, s93
	v_cvt_pk_bf16_f32 v218, v58, v59
	v_cvt_pk_bf16_f32 v219, v60, v61
	v_cvt_pk_bf16_f32 v182, v74, v75
	v_cvt_pk_bf16_f32 v183, v76, v77
	v_mfma_f32_32x32x16_bf16 v[98:113], v[162:165], v[158:161], v[98:113]
	v_cvt_pk_bf16_f32 v220, v62, v63
	v_cvt_pk_bf16_f32 v221, v64, v65
	v_cvt_pk_bf16_f32 v184, v78, v79
	v_cvt_pk_bf16_f32 v185, v80, v81
	v_add_f32_e32 v3, v3, v16
	v_add_f32_e32 v246, v246, v3
	s_branch .Lmla_ss2_loop
